# down-projection expert loop: the first fragment wait after a pass epilogue counts the wave's own epilogue stores instead of draining them; redundant top-of-step waits removed
# speedup vs baseline: 1.0081x; 1.0081x over previous
.LBB0_1430:
	v_or_b32_e32 v244, v0, v232
	s_mov_b64 s[42:43], s[50:51]
	s_mov_b64 s[64:65], s[48:49]
	v_mov_b32_e32 v0, v239
	global_load_dwordx4 v[200:203], v244, s[30:31] offset:16
	global_load_dwordx4 v[196:199], v244, s[30:31]
	global_load_dwordx4 v[2:5], v0, s[64:65] nt
	global_load_dwordx4 v[10:13], v0, s[42:43] nt
	v_lshl_add_u64 v[6:7], s[64:65], 0, v[0:1]
	v_add_co_u32_e32 v6, vcc, s85, v6
	v_lshl_add_u64 v[14:15], s[42:43], 0, v[0:1]
	s_nop 0
	v_addc_co_u32_e32 v7, vcc, 0, v7, vcc
	v_add_co_u32_e32 v14, vcc, s85, v14
	global_load_dwordx4 v[6:9], v[6:7], off nt
	s_nop 0
	v_addc_co_u32_e32 v15, vcc, 0, v15, vcc
	global_load_dwordx4 v[14:17], v[14:15], off nt
	s_mov_b64 s[42:43], s[52:53]
	s_mov_b64 s[64:65], s[54:55]
	v_mov_b32_e32 v0, v239
	global_load_dwordx4 v[160:163], v0, s[42:43] nt
	global_load_dwordx4 v[168:171], v0, s[64:65] nt
	v_lshl_add_u64 v[18:19], s[42:43], 0, v[0:1]
	v_add_co_u32_e32 v18, vcc, s85, v18
	v_add_u32_e32 v245, 0, v240
	s_nop 0
	v_addc_co_u32_e32 v19, vcc, 0, v19, vcc
	global_load_dwordx4 v[164:167], v[18:19], off nt
	v_lshl_add_u64 v[18:19], s[64:65], 0, v[0:1]
	v_add_co_u32_e32 v18, vcc, s85, v18
	s_mov_b64 s[42:43], s[60:61]
	s_nop 0
	v_addc_co_u32_e32 v19, vcc, 0, v19, vcc
	s_mov_b64 s[64:65], s[58:59]
	global_load_dwordx4 v[172:175], v[18:19], off nt
	s_min_i32 s45, s56, 0x400
	s_sub_i32 s25, s45, s84
	s_cmp_lt_i32 s33, s25
	v_add_u32_e32 v246, 0, v241
	s_mov_b32 s87, 0
	v_add_u32_e32 v247, s38, v246
	s_movk_i32 s45, 0x80
	s_mov_b32 s88, 2
	s_waitcnt vmcnt(5)
	v_cvt_pk_bf16_f32 v0, v2, v6
	v_mov_b32_e32 v6, v1
	s_waitcnt vmcnt(4)
	v_cvt_pk_bf16_f32 v2, v10, v14
	ds_write2_b32 v245, v0, v2 offset1:8
	v_cvt_pk_bf16_f32 v0, v3, v7
	v_cvt_pk_bf16_f32 v2, v11, v15
	v_add_u32_e32 v3, 0x400, v245
	ds_write2_b32 v3, v0, v2 offset0:32 offset1:40
	v_cvt_pk_bf16_f32 v0, v4, v8
	v_cvt_pk_bf16_f32 v2, v12, v16
	v_add_u32_e32 v3, 0x800, v245
	ds_write2_b32 v3, v0, v2 offset0:64 offset1:72
	v_cvt_pk_bf16_f32 v0, v5, v9
	v_cvt_pk_bf16_f32 v2, v13, v17
	v_add_u32_e32 v3, 0xc00, v245
	ds_write2_b32 v3, v0, v2 offset0:96 offset1:104
	v_mov_b32_e32 v0, v239
	global_load_dwordx4 v[176:179], v0, s[64:65] nt
	global_load_dwordx4 v[184:187], v0, s[42:43] nt
	v_lshl_add_u64 v[2:3], s[64:65], 0, v[0:1]
	v_add_co_u32_e32 v2, vcc, s85, v2
	v_mov_b32_e32 v14, v1
	s_nop 0
	v_addc_co_u32_e32 v3, vcc, 0, v3, vcc
	global_load_dwordx4 v[180:183], v[2:3], off nt
	v_lshl_add_u64 v[2:3], s[42:43], 0, v[0:1]
	v_add_co_u32_e32 v2, vcc, s85, v2
	v_mov_b32_e32 v15, v1
	s_nop 0
	v_addc_co_u32_e32 v3, vcc, 0, v3, vcc
	global_load_dwordx4 v[188:191], v[2:3], off nt
	s_cselect_b64 s[64:65], -1, 0
	v_mov_b32_e32 v0, v1
	v_mov_b32_e32 v2, v1
	v_mov_b32_e32 v3, v1
	v_mov_b32_e32 v4, v1
	v_mov_b32_e32 v5, v1
	v_mov_b32_e32 v7, v1
	v_mov_b32_e32 v8, v1
	v_mov_b32_e32 v9, v1
	v_mov_b32_e32 v10, v1
	v_mov_b32_e32 v11, v1
	v_mov_b32_e32 v12, v1
	v_mov_b32_e32 v13, v1
	v_mov_b32_e32 v16, 0
	s_cmp_lt_i32 s39, s25
	v_mov_b64_e32 v[46:47], v[14:15]
	v_mov_b64_e32 v[62:63], v[14:15]
	v_mov_b64_e32 v[78:79], v[14:15]
	v_mov_b64_e32 v[94:95], v[14:15]
	v_mov_b64_e32 v[110:111], v[14:15]
	v_mov_b64_e32 v[126:127], v[14:15]
	v_mov_b64_e32 v[142:143], v[14:15]
	v_mov_b64_e32 v[158:159], v[14:15]
	s_cselect_b64 s[66:67], -1, 0
	v_mov_b64_e32 v[44:45], v[12:13]
	v_mov_b64_e32 v[42:43], v[10:11]
	v_mov_b64_e32 v[40:41], v[8:9]
	v_mov_b64_e32 v[38:39], v[6:7]
	v_mov_b64_e32 v[36:37], v[4:5]
	v_mov_b64_e32 v[34:35], v[2:3]
	v_mov_b64_e32 v[32:33], v[0:1]
	v_mov_b64_e32 v[60:61], v[12:13]
	v_mov_b64_e32 v[58:59], v[10:11]
	v_mov_b64_e32 v[56:57], v[8:9]
	v_mov_b64_e32 v[54:55], v[6:7]
	v_mov_b64_e32 v[52:53], v[4:5]
	v_mov_b64_e32 v[50:51], v[2:3]
	v_mov_b64_e32 v[48:49], v[0:1]
	v_mov_b64_e32 v[76:77], v[12:13]
	v_mov_b64_e32 v[74:75], v[10:11]
	v_mov_b64_e32 v[72:73], v[8:9]
	v_mov_b64_e32 v[70:71], v[6:7]
	v_mov_b64_e32 v[68:69], v[4:5]
	v_mov_b64_e32 v[66:67], v[2:3]
	v_mov_b64_e32 v[64:65], v[0:1]
	v_mov_b64_e32 v[92:93], v[12:13]
	v_mov_b64_e32 v[90:91], v[10:11]
	v_mov_b64_e32 v[88:89], v[8:9]
	v_mov_b64_e32 v[86:87], v[6:7]
	v_mov_b64_e32 v[84:85], v[4:5]
	v_mov_b64_e32 v[82:83], v[2:3]
	v_mov_b64_e32 v[80:81], v[0:1]
	v_mov_b64_e32 v[108:109], v[12:13]
	v_mov_b64_e32 v[106:107], v[10:11]
	v_mov_b64_e32 v[104:105], v[8:9]
	v_mov_b64_e32 v[102:103], v[6:7]
	v_mov_b64_e32 v[100:101], v[4:5]
	v_mov_b64_e32 v[98:99], v[2:3]
	v_mov_b64_e32 v[96:97], v[0:1]
	v_mov_b64_e32 v[124:125], v[12:13]
	v_mov_b64_e32 v[122:123], v[10:11]
	v_mov_b64_e32 v[120:121], v[8:9]
	v_mov_b64_e32 v[118:119], v[6:7]
	v_mov_b64_e32 v[116:117], v[4:5]
	v_mov_b64_e32 v[114:115], v[2:3]
	v_mov_b64_e32 v[112:113], v[0:1]
	v_mov_b64_e32 v[140:141], v[12:13]
	v_mov_b64_e32 v[138:139], v[10:11]
	v_mov_b64_e32 v[136:137], v[8:9]
	v_mov_b64_e32 v[134:135], v[6:7]
	v_mov_b64_e32 v[132:133], v[4:5]
	v_mov_b64_e32 v[130:131], v[2:3]
	v_mov_b64_e32 v[128:129], v[0:1]
	v_mov_b64_e32 v[156:157], v[12:13]
	v_mov_b64_e32 v[154:155], v[10:11]
	v_mov_b64_e32 v[152:153], v[8:9]
	v_mov_b64_e32 v[150:151], v[6:7]
	v_mov_b64_e32 v[148:149], v[4:5]
	v_mov_b64_e32 v[146:147], v[2:3]
	v_mov_b64_e32 v[144:145], v[0:1]
	v_mov_b32_e32 v17, v16
	v_mov_b32_e32 v18, v16
	v_mov_b32_e32 v19, v16
	v_mov_b32_e32 v20, v16
	v_mov_b32_e32 v21, v16
	v_mov_b32_e32 v22, v16
	v_mov_b32_e32 v23, v16
	v_mov_b32_e32 v24, v16
	v_mov_b32_e32 v25, v16
	v_mov_b32_e32 v26, v16
	v_mov_b32_e32 v27, v16
	v_mov_b32_e32 v28, v16
	v_mov_b32_e32 v29, v16
	v_mov_b32_e32 v30, v16
	v_mov_b32_e32 v31, v16
	s_mov_b32 s91, 0
	s_mov_b32 s92, 0
	s_waitcnt vmcnt(4)
	s_branch .LBB0_1433

.LBB0_1433:
	s_add_i32 s25, s87, 1
	s_cmp_lg_u32 s87, 2
	s_cselect_b32 s70, s25, 0
	s_mul_i32 s25, s70, 0x4800
	s_add_i32 s90, s25, 0
	s_add_i32 s25, s88, 1
	s_cmp_lt_u32 s25, s80
	s_cselect_b32 s25, s25, 0
	s_lshr_b32 s42, s25, 2
	s_add_i32 s42, s42, s79
	s_and_b32 s42, s42, s78
	s_add_i32 s42, s42, s77
	s_lshl_b32 s25, s25, 16
	s_lshl_b32 s42, s42, 7
	s_and_b32 s25, s25, 0x30000
	s_add_i32 s56, s42, s25
	v_add_u32_e32 v0, s90, v240
	v_cvt_pk_bf16_f32 v2, v160, v164
	v_cvt_pk_bf16_f32 v3, v168, v172
	s_lshl_b64 s[42:43], s[56:57], 2
	s_waitcnt lgkmcnt(0)
	s_barrier
	ds_write2_b32 v0, v2, v3 offset1:8
	v_cvt_pk_bf16_f32 v2, v161, v165
	v_cvt_pk_bf16_f32 v3, v169, v173
	v_add_u32_e32 v4, 0x400, v0
	s_add_u32 s42, s82, s42
	ds_write2_b32 v4, v2, v3 offset0:32 offset1:40
	v_cvt_pk_bf16_f32 v2, v162, v166
	v_cvt_pk_bf16_f32 v3, v170, v174
	v_add_u32_e32 v4, 0x800, v0
	s_addc_u32 s43, s83, s43
	ds_write2_b32 v4, v2, v3 offset0:64 offset1:72
	v_cvt_pk_bf16_f32 v2, v163, v167
	v_cvt_pk_bf16_f32 v3, v171, v175
	v_add_u32_e32 v0, 0xc00, v0
	s_add_u32 s68, s42, 0x10000
	ds_write2_b32 v0, v2, v3 offset0:96 offset1:104
	s_addc_u32 s69, s43, 0
	v_mov_b32_e32 v0, v239
	global_load_dwordx4 v[160:163], v0, s[42:43] nt
	global_load_dwordx4 v[168:171], v0, s[68:69] nt
	v_lshl_add_u64 v[2:3], s[42:43], 0, v[0:1]
	v_add_co_u32_e32 v2, vcc, s85, v2
	s_sub_i32 s42, s45, 64
	s_nop 0
	v_addc_co_u32_e32 v3, vcc, 0, v3, vcc
	global_load_dwordx4 v[164:167], v[2:3], off nt
	v_lshl_add_u64 v[2:3], s[68:69], 0, v[0:1]
	v_add_co_u32_e32 v2, vcc, s85, v2
	s_add_i32 s25, s88, -1
	s_nop 0
	v_addc_co_u32_e32 v3, vcc, 0, v3, vcc
	global_load_dwordx4 v[172:175], v[2:3], off nt
	s_and_b32 s42, s42, 0xc0
	s_cmp_lt_u32 s25, s80
	s_cselect_b32 s25, s42, 0
	s_add_u32 s68, s25, s30
	v_cndmask_b32_e64 v0, 0, 1, s[64:65]
	s_addc_u32 s69, 0, s31
	s_mul_i32 s56, s87, 0x4800
	v_cmp_ne_u32_e64 s[42:43], 1, v0
	s_andn2_b64 vcc, exec, s[64:65]
	s_cbranch_vccnz .LBB0_1435
	s_cmp_eq_u32 s91, 0
	s_cbranch_scc1 .Ldn_w6
	s_add_i32 s91, s91, s92
	s_mov_b32 s92, 0
	s_cmp_eq_u32 s91, 4
	s_cbranch_scc1 .Ldn_w10
	s_cmp_eq_u32 s91, 5
	s_cbranch_scc1 .Ldn_w11
	s_cmp_eq_u32 s91, 8
	s_cbranch_scc1 .Ldn_w14
	s_waitcnt vmcnt(15)
	s_branch .Ldn_wd
.Ldn_w14:
	s_waitcnt vmcnt(14)
	s_branch .Ldn_wd
.Ldn_w11:
	s_waitcnt vmcnt(11)
	s_branch .Ldn_wd
.Ldn_w10:
	s_waitcnt vmcnt(10)
	s_branch .Ldn_wd

.Ldn_wd:
	s_mov_b32 s91, 0
	v_cvt_pk_f32_fp8_e32 v[6:7], v212
	v_cvt_pk_f32_fp8_sdwa v[8:9], v212 src0_sel:WORD_1
	v_cvt_pk_f32_fp8_e32 v[10:11], v213
	v_cvt_pk_f32_fp8_sdwa v[12:13], v213 src0_sel:WORD_1
	v_add_u32_e32 v0, s56, v246
	ds_read_b128 v[2:5], v0
	v_cvt_pk_bf16_f32 v6, v6, v7
	v_cvt_pk_bf16_f32 v7, v8, v9
	v_cvt_pk_bf16_f32 v8, v10, v11
	v_cvt_pk_bf16_f32 v9, v12, v13
	ds_read_b128 v[10:13], v0 offset:4608
	ds_read_b128 v[216:219], v0 offset:9216
	ds_read_b128 v[248:251], v0 offset:13824
	s_waitcnt lgkmcnt(3)
	v_mfma_f32_32x32x16_bf16 v[144:159], v[2:5], v[6:9], v[144:159]
	v_cvt_pk_f32_fp8_e32 v[14:15], v209
	s_waitcnt lgkmcnt(2)
	v_mfma_f32_32x32x16_bf16 v[128:143], v[10:13], v[6:9], v[128:143]
	s_waitcnt lgkmcnt(1)
	v_mfma_f32_32x32x16_bf16 v[112:127], v[216:219], v[6:9], v[112:127]
	s_waitcnt lgkmcnt(0)
	v_mfma_f32_32x32x16_bf16 v[96:111], v[248:251], v[6:9], v[96:111]
	v_cvt_pk_f32_fp8_e32 v[6:7], v208
	v_cvt_pk_f32_fp8_sdwa v[8:9], v208 src0_sel:WORD_1
	v_cvt_pk_f32_fp8_sdwa v[208:209], v209 src0_sel:WORD_1
	v_cvt_pk_bf16_f32 v6, v6, v7
	v_cvt_pk_bf16_f32 v7, v8, v9
	v_cvt_pk_bf16_f32 v8, v14, v15
	v_cvt_pk_bf16_f32 v9, v208, v209
	v_cvt_pk_f32_fp8_e32 v[14:15], v211
	v_cvt_pk_f32_fp8_sdwa v[208:209], v211 src0_sel:WORD_1
	v_mfma_f32_32x32x16_bf16 v[80:95], v[2:5], v[6:9], v[80:95]
	ds_read_b128 v[2:5], v0 offset:16
	v_mfma_f32_32x32x16_bf16 v[64:79], v[10:13], v[6:9], v[64:79]
	v_cvt_pk_f32_fp8_e32 v[10:11], v215
	v_cvt_pk_f32_fp8_sdwa v[12:13], v215 src0_sel:WORD_1
	v_mfma_f32_32x32x16_bf16 v[48:63], v[216:219], v[6:9], v[48:63]
	ds_read_b128 v[216:219], v0 offset:13840
	v_mfma_f32_32x32x16_bf16 v[32:47], v[248:251], v[6:9], v[32:47]
	v_cvt_pk_f32_fp8_e32 v[6:7], v214
	v_cvt_pk_f32_fp8_sdwa v[8:9], v214 src0_sel:WORD_1
	ds_read_b128 v[212:215], v0 offset:9232
	v_cvt_pk_bf16_f32 v6, v6, v7
	v_cvt_pk_bf16_f32 v7, v8, v9
	v_cvt_pk_bf16_f32 v8, v10, v11
	v_cvt_pk_bf16_f32 v9, v12, v13
	ds_read_b128 v[10:13], v0 offset:4624
	s_waitcnt lgkmcnt(3)
	v_mfma_f32_32x32x16_bf16 v[144:159], v[2:5], v[6:9], v[144:159]
	s_waitcnt lgkmcnt(0)
	v_mfma_f32_32x32x16_bf16 v[128:143], v[10:13], v[6:9], v[128:143]
	v_mfma_f32_32x32x16_bf16 v[112:127], v[212:215], v[6:9], v[112:127]
	v_mfma_f32_32x32x16_bf16 v[96:111], v[216:219], v[6:9], v[96:111]
	v_cvt_pk_f32_fp8_e32 v[6:7], v210
	v_cvt_pk_f32_fp8_sdwa v[8:9], v210 src0_sel:WORD_1
	v_cvt_pk_bf16_f32 v6, v6, v7
	v_cvt_pk_bf16_f32 v7, v8, v9
	v_cvt_pk_bf16_f32 v8, v14, v15
	v_cvt_pk_bf16_f32 v9, v208, v209
	ds_read_b128 v[208:211], v0 offset:9248
	v_cvt_pk_f32_fp8_e32 v[14:15], v193
	v_mfma_f32_32x32x16_bf16 v[80:95], v[2:5], v[6:9], v[80:95]
	ds_read_b128 v[2:5], v0 offset:32
	v_mfma_f32_32x32x16_bf16 v[64:79], v[10:13], v[6:9], v[64:79]
	v_cvt_pk_f32_fp8_e32 v[10:11], v205
	v_cvt_pk_f32_fp8_sdwa v[12:13], v205 src0_sel:WORD_1
	v_mfma_f32_32x32x16_bf16 v[48:63], v[212:215], v[6:9], v[48:63]
	ds_read_b128 v[212:215], v0 offset:13856
	v_mfma_f32_32x32x16_bf16 v[32:47], v[216:219], v[6:9], v[32:47]
	v_cvt_pk_f32_fp8_e32 v[6:7], v204
	v_cvt_pk_f32_fp8_sdwa v[8:9], v204 src0_sel:WORD_1
	v_cvt_pk_bf16_f32 v6, v6, v7
	v_cvt_pk_bf16_f32 v7, v8, v9
	v_cvt_pk_bf16_f32 v8, v10, v11
	v_cvt_pk_bf16_f32 v9, v12, v13
	ds_read_b128 v[10:13], v0 offset:4640
	s_waitcnt lgkmcnt(2)
	v_mfma_f32_32x32x16_bf16 v[144:159], v[2:5], v[6:9], v[144:159]
	s_waitcnt lgkmcnt(0)
	v_mfma_f32_32x32x16_bf16 v[128:143], v[10:13], v[6:9], v[128:143]
	v_mfma_f32_32x32x16_bf16 v[112:127], v[208:211], v[6:9], v[112:127]
	v_mfma_f32_32x32x16_bf16 v[96:111], v[212:215], v[6:9], v[96:111]
	v_cvt_pk_f32_fp8_e32 v[6:7], v192
	v_cvt_pk_f32_fp8_sdwa v[8:9], v192 src0_sel:WORD_1
	v_cvt_pk_f32_fp8_sdwa v[192:193], v193 src0_sel:WORD_1
	v_cvt_pk_bf16_f32 v6, v6, v7
	v_cvt_pk_bf16_f32 v7, v8, v9
	v_cvt_pk_bf16_f32 v8, v14, v15
	v_cvt_pk_bf16_f32 v9, v192, v193
	v_cvt_pk_f32_fp8_e32 v[14:15], v195
	v_cvt_pk_f32_fp8_sdwa v[192:193], v195 src0_sel:WORD_1
	v_mfma_f32_32x32x16_bf16 v[80:95], v[2:5], v[6:9], v[80:95]
	ds_read_b128 v[2:5], v0 offset:48
	v_mfma_f32_32x32x16_bf16 v[64:79], v[10:13], v[6:9], v[64:79]
	v_cvt_pk_f32_fp8_e32 v[10:11], v207
	v_cvt_pk_f32_fp8_sdwa v[12:13], v207 src0_sel:WORD_1
	v_mfma_f32_32x32x16_bf16 v[48:63], v[208:211], v[6:9], v[48:63]
	ds_read_b128 v[208:211], v0 offset:13872
	v_mfma_f32_32x32x16_bf16 v[32:47], v[212:215], v[6:9], v[32:47]
	v_cvt_pk_f32_fp8_e32 v[6:7], v206
	v_cvt_pk_f32_fp8_sdwa v[8:9], v206 src0_sel:WORD_1
	ds_read_b128 v[204:207], v0 offset:9264
	v_cvt_pk_bf16_f32 v6, v6, v7
	v_cvt_pk_bf16_f32 v7, v8, v9
	v_cvt_pk_bf16_f32 v8, v10, v11
	v_cvt_pk_bf16_f32 v9, v12, v13
	ds_read_b128 v[10:13], v0 offset:4656
	s_waitcnt lgkmcnt(3)
	v_mfma_f32_32x32x16_bf16 v[144:159], v[2:5], v[6:9], v[144:159]
	s_waitcnt lgkmcnt(0)
	v_mfma_f32_32x32x16_bf16 v[128:143], v[10:13], v[6:9], v[128:143]
	v_mfma_f32_32x32x16_bf16 v[112:127], v[204:207], v[6:9], v[112:127]
	v_mfma_f32_32x32x16_bf16 v[96:111], v[208:211], v[6:9], v[96:111]
	v_cvt_pk_f32_fp8_e32 v[6:7], v194
	v_cvt_pk_f32_fp8_sdwa v[8:9], v194 src0_sel:WORD_1
	v_cvt_pk_bf16_f32 v6, v6, v7
	v_cvt_pk_bf16_f32 v7, v8, v9
	v_cvt_pk_bf16_f32 v8, v14, v15
	v_cvt_pk_bf16_f32 v9, v192, v193
	s_nop 1
	v_mfma_f32_32x32x16_bf16 v[80:95], v[2:5], v[6:9], v[80:95]
	v_mfma_f32_32x32x16_bf16 v[64:79], v[10:13], v[6:9], v[64:79]
	v_mfma_f32_32x32x16_bf16 v[48:63], v[204:207], v[6:9], v[48:63]
	v_mfma_f32_32x32x16_bf16 v[32:47], v[208:211], v[6:9], v[32:47]

.LBB0_1437:
	v_mov_b32_e32 v0, v242
	global_load_dwordx4 v[204:207], v0, s[70:71] offset:16
	global_load_dwordx4 v[212:215], v0, s[70:71]
	v_mov_b32_e32 v0, v243
	s_add_i32 s25, s38, s90
	global_load_dwordx4 v[192:195], v0, s[70:71] offset:16
	global_load_dwordx4 v[208:211], v0, s[70:71]
	v_add_u32_e32 v0, s25, v241
	ds_read_b128 v[196:199], v0
	s_waitcnt vmcnt(9)
	v_cvt_pk_f32_fp8_e32 v[6:7], v2
	v_cvt_pk_f32_fp8_sdwa v[8:9], v2 src0_sel:WORD_1
	v_cvt_pk_f32_fp8_e32 v[14:15], v3
	v_cvt_pk_f32_fp8_sdwa v[2:3], v3 src0_sel:WORD_1
	v_cvt_pk_bf16_f32 v6, v6, v7
	v_cvt_pk_bf16_f32 v7, v8, v9
	v_cvt_pk_bf16_f32 v8, v14, v15
	v_cvt_pk_bf16_f32 v9, v2, v3
	v_cvt_pk_f32_fp8_e32 v[2:3], v4
	v_cvt_pk_f32_fp8_sdwa v[14:15], v5 src0_sel:WORD_1
	s_waitcnt lgkmcnt(0)
	v_mfma_f32_32x32x16_bf16 v[16:31], v[196:199], v[6:9], v[16:31]
	v_cvt_pk_f32_fp8_sdwa v[6:7], v4 src0_sel:WORD_1
	v_cvt_pk_f32_fp8_e32 v[8:9], v5
	v_cvt_pk_bf16_f32 v2, v2, v3
	v_cvt_pk_bf16_f32 v5, v14, v15
	v_cvt_pk_bf16_f32 v3, v6, v7
	v_mov_b32_e32 v6, v244
	v_cvt_pk_bf16_f32 v4, v8, v9
	global_load_dwordx4 v[196:199], v6, s[70:71]
	ds_read_b128 v[6:9], v0 offset:16
	ds_read_b128 v[200:203], v0 offset:32
	s_waitcnt lgkmcnt(1)
	v_mfma_f32_32x32x16_bf16 v[16:31], v[6:9], v[2:5], v[16:31]
	s_waitcnt vmcnt(9)
	v_cvt_pk_f32_fp8_e32 v[2:3], v10
	v_cvt_pk_f32_fp8_sdwa v[4:5], v10 src0_sel:WORD_1
	v_cvt_pk_f32_fp8_e32 v[6:7], v11
	v_cvt_pk_f32_fp8_sdwa v[8:9], v11 src0_sel:WORD_1
	v_cvt_pk_bf16_f32 v2, v2, v3
	v_cvt_pk_bf16_f32 v3, v4, v5
	v_cvt_pk_bf16_f32 v4, v6, v7
	v_cvt_pk_bf16_f32 v5, v8, v9
	v_cvt_pk_f32_fp8_e32 v[6:7], v13
	v_cvt_pk_f32_fp8_sdwa v[8:9], v13 src0_sel:WORD_1
	s_waitcnt lgkmcnt(0)
	v_mfma_f32_32x32x16_bf16 v[16:31], v[200:203], v[2:5], v[16:31]
	v_cvt_pk_f32_fp8_e32 v[2:3], v12
	v_cvt_pk_f32_fp8_sdwa v[4:5], v12 src0_sel:WORD_1
	s_add_i32 s56, s88, -2
	s_and_b32 s88, s56, 2
	v_cvt_pk_bf16_f32 v2, v2, v3
	v_cvt_pk_bf16_f32 v3, v4, v5
	v_cvt_pk_bf16_f32 v4, v6, v7
	v_mov_b32_e32 v6, v244
	global_load_dwordx4 v[200:203], v6, s[70:71] offset:16
	v_cvt_pk_bf16_f32 v5, v8, v9
	ds_read_b128 v[6:9], v0 offset:48
	s_cmp_eq_u32 s88, 0
	s_waitcnt lgkmcnt(0)
	v_mfma_f32_32x32x16_bf16 v[16:31], v[6:9], v[2:5], v[16:31]
	s_cbranch_scc1 .LBB0_1432
	s_lshr_b32 s25, s56, 2
	v_mbcnt_lo_u32_b32 v0, -1, 0
	v_mbcnt_hi_u32_b32 v0, -1, v0
	s_add_i32 s25, s25, s79
	v_and_b32_e32 v248, 31, v0
	v_ashrrev_i32_e32 v0, 5, v0
	s_and_b32 s56, s25, s78
	v_lshlrev_b32_e32 v218, 4, v0
	s_add_i32 s56, s56, s77
	s_and_b64 vcc, exec, s[42:43]
	v_ashrrev_i32_e32 v219, 31, v218
	s_cbranch_vccnz .LBB0_1442
	v_or_b32_e32 v0, s86, v248
	v_lshl_add_u32 v4, v0, 2, 0
	ds_read2st64_b32 v[14:15], v4 offset0:216 offset1:232
	v_mov_b32_e32 v6, v1
	v_mov_b32_e32 v7, v1
	s_lshl_b32 s25, s56, 7
	s_add_u32 s42, s12, s25
	s_waitcnt lgkmcnt(0)
	v_mov_b32_e32 v0, v14
	v_lshlrev_b64 v[216:217], 10, v[0:1]
	v_mul_f32_e32 v0, v144, v15
	v_mul_f32_e32 v5, v148, v15
	v_cvt_pk_fp8_f32 v6, v0, v5
	v_mul_f32_e32 v8, v145, v15
	v_mul_f32_e32 v9, v149, v15
	v_mul_f32_e32 v10, v152, v15
	v_mul_f32_e32 v11, v156, v15
	v_cvt_pk_fp8_f32 v7, v8, v9
	v_cvt_pk_fp8_f32 v6, v10, v11 op_sel:[0,0,1]
	v_mul_f32_e32 v0, v128, v15
	v_mul_f32_e32 v5, v132, v15
	v_mov_b32_e32 v10, v1
	v_cvt_pk_fp8_f32 v10, v0, v5
	v_mul_f32_e32 v12, v153, v15
	v_mul_f32_e32 v13, v157, v15
	v_mul_f32_e32 v14, v146, v15
	v_mul_f32_e32 v144, v150, v15
	v_mul_f32_e32 v147, v147, v15
	v_mul_f32_e32 v148, v151, v15
	v_mov_b32_e32 v8, v1
	v_mov_b32_e32 v9, v1
	v_cvt_pk_fp8_f32 v7, v12, v13 op_sel:[0,0,1]
	v_mul_f32_e32 v12, v129, v15
	v_mul_f32_e32 v13, v133, v15
	v_mov_b32_e32 v11, v1
	v_cvt_pk_fp8_f32 v8, v14, v144
	v_cvt_pk_fp8_f32 v9, v147, v148
	v_mul_f32_e32 v14, v136, v15
	v_mul_f32_e32 v128, v140, v15
	v_mul_f32_e32 v130, v130, v15
	v_mul_f32_e32 v133, v134, v15
	v_mul_f32_e32 v131, v131, v15
	v_mul_f32_e32 v135, v135, v15
	v_cvt_pk_fp8_f32 v11, v12, v13
	v_mov_b32_e32 v12, v1
	v_mov_b32_e32 v13, v1
	v_cvt_pk_fp8_f32 v12, v130, v133
	v_cvt_pk_fp8_f32 v13, v131, v135
	v_cvt_pk_fp8_f32 v10, v14, v128 op_sel:[0,0,1]
	v_mul_f32_e32 v0, v112, v15
	v_mul_f32_e32 v5, v116, v15
	v_mul_f32_e32 v14, v120, v15
	v_mul_f32_e32 v116, v124, v15
	v_mul_f32_e32 v120, v113, v15
	v_mul_f32_e32 v117, v117, v15
	v_mul_f32_e32 v124, v125, v15
	v_mul_f32_e32 v125, v114, v15
	v_mul_f32_e32 v118, v118, v15
	v_mul_f32_e32 v128, v115, v15
	v_mul_f32_e32 v119, v119, v15
	v_mov_b32_e32 v112, v1
	v_mov_b32_e32 v113, v1
	v_mov_b32_e32 v114, v1
	v_mov_b32_e32 v115, v1
	v_cvt_pk_fp8_f32 v112, v0, v5
	v_cvt_pk_fp8_f32 v113, v120, v117
	v_cvt_pk_fp8_f32 v114, v125, v118
	v_cvt_pk_fp8_f32 v115, v128, v119
	v_mul_f32_e32 v145, v154, v15
	v_mul_f32_e32 v146, v158, v15
	v_mul_f32_e32 v149, v155, v15
	v_mul_f32_e32 v150, v159, v15
	v_cvt_pk_fp8_f32 v8, v145, v146 op_sel:[0,0,1]
	v_cvt_pk_fp8_f32 v9, v149, v150 op_sel:[0,0,1]
	v_mul_f32_e32 v129, v137, v15
	v_mul_f32_e32 v132, v141, v15
	v_mul_f32_e32 v134, v138, v15
	v_mul_f32_e32 v136, v142, v15
	v_mul_f32_e32 v137, v139, v15
	v_mul_f32_e32 v138, v143, v15
	s_addc_u32 s43, s13, 0
	v_cvt_pk_fp8_f32 v11, v129, v132 op_sel:[0,0,1]
	v_cvt_pk_fp8_f32 v12, v134, v136 op_sel:[0,0,1]
	v_cvt_pk_fp8_f32 v13, v137, v138 op_sel:[0,0,1]
	v_mul_f32_e32 v121, v121, v15
	v_mul_f32_e32 v122, v122, v15
	v_mul_f32_e32 v126, v126, v15
	v_mul_f32_e32 v123, v123, v15
	v_mul_f32_e32 v127, v127, v15
	v_lshl_add_u64 v[2:3], s[42:43], 0, v[218:219]
	v_cvt_pk_fp8_f32 v112, v14, v116 op_sel:[0,0,1]
	v_cvt_pk_fp8_f32 v113, v121, v124 op_sel:[0,0,1]
	v_cvt_pk_fp8_f32 v114, v122, v126 op_sel:[0,0,1]
	v_cvt_pk_fp8_f32 v115, v123, v127 op_sel:[0,0,1]
	v_lshl_add_u64 v[116:117], v[2:3], 0, v[216:217]
	global_store_dwordx4 v[116:117], v[6:9], off
	global_store_dwordx4 v[116:117], v[10:13], off offset:32
	global_store_dwordx4 v[116:117], v[112:115], off offset:64
	v_mul_f32_e32 v8, v97, v15
	v_mul_f32_e32 v9, v101, v15
	v_mov_b32_e32 v7, v1
	v_mul_f32_e32 v0, v96, v15
	v_mul_f32_e32 v5, v100, v15
	v_mul_f32_e32 v14, v98, v15
	v_mul_f32_e32 v96, v102, v15
	v_mul_f32_e32 v99, v99, v15
	v_mul_f32_e32 v100, v103, v15
	v_mov_b32_e32 v6, v1
	v_cvt_pk_fp8_f32 v7, v8, v9
	v_mov_b32_e32 v8, v1
	v_mov_b32_e32 v9, v1
	v_cvt_pk_fp8_f32 v6, v0, v5
	v_cvt_pk_fp8_f32 v8, v14, v96
	v_cvt_pk_fp8_f32 v9, v99, v100
	v_mul_f32_e32 v10, v104, v15
	v_mul_f32_e32 v11, v108, v15
	v_mul_f32_e32 v12, v105, v15
	v_mul_f32_e32 v13, v109, v15
	v_mul_f32_e32 v97, v106, v15
	v_mul_f32_e32 v98, v110, v15
	v_mul_f32_e32 v101, v107, v15
	v_mul_f32_e32 v15, v111, v15
	v_cvt_pk_fp8_f32 v6, v10, v11 op_sel:[0,0,1]
	v_cvt_pk_fp8_f32 v7, v12, v13 op_sel:[0,0,1]
	v_cvt_pk_fp8_f32 v8, v97, v98 op_sel:[0,0,1]
	v_cvt_pk_fp8_f32 v9, v101, v15 op_sel:[0,0,1]
	s_andn2_b64 vcc, exec, s[66:67]
	global_store_dwordx4 v[116:117], v[6:9], off offset:96
	s_mov_b32 s91, 4
	s_cbranch_vccnz .LBB0_1441
	v_add_u32_e32 v0, 0x80, v4
	ds_read2st64_b32 v[14:15], v0 offset0:216 offset1:232
	s_waitcnt lgkmcnt(0)
	v_mov_b32_e32 v0, v14
	v_lshlrev_b64 v[4:5], 10, v[0:1]
	v_mul_f32_e32 v6, v80, v15
	v_mul_f32_e32 v7, v84, v15
	v_lshl_add_u64 v[96:97], v[2:3], 0, v[4:5]
	v_mov_b32_e32 v2, v1
	v_cvt_pk_fp8_f32 v2, v6, v7
	v_mul_f32_e32 v0, v81, v15
	v_mul_f32_e32 v4, v85, v15
	v_mov_b32_e32 v3, v1
	v_mul_f32_e32 v8, v88, v15
	v_mul_f32_e32 v9, v92, v15
	v_mul_f32_e32 v5, v82, v15
	v_mul_f32_e32 v12, v86, v15
	v_cvt_pk_fp8_f32 v3, v0, v4
	v_mov_b32_e32 v4, v1
	v_mul_f32_e32 v0, v64, v15
	v_mul_f32_e32 v7, v68, v15
	v_mov_b32_e32 v6, v1
	v_cvt_pk_fp8_f32 v4, v5, v12
	v_cvt_pk_fp8_f32 v2, v8, v9 op_sel:[0,0,1]
	v_mul_f32_e32 v8, v65, v15
	v_mul_f32_e32 v9, v69, v15
	v_cvt_pk_fp8_f32 v6, v0, v7
	v_mov_b32_e32 v7, v1
	v_cvt_pk_fp8_f32 v7, v8, v9
	v_mul_f32_e32 v10, v89, v15
	v_mul_f32_e32 v11, v93, v15
	v_mul_f32_e32 v13, v90, v15
	v_mul_f32_e32 v14, v94, v15
	v_cvt_pk_fp8_f32 v3, v10, v11 op_sel:[0,0,1]
	v_mul_f32_e32 v10, v72, v15
	v_mul_f32_e32 v11, v76, v15
	v_cvt_pk_fp8_f32 v4, v13, v14 op_sel:[0,0,1]
	v_mul_f32_e32 v12, v73, v15
	v_mul_f32_e32 v13, v77, v15
	v_cvt_pk_fp8_f32 v6, v10, v11 op_sel:[0,0,1]
	v_mul_f32_e32 v0, v48, v15
	v_mul_f32_e32 v11, v52, v15
	v_mov_b32_e32 v10, v1
	v_cvt_pk_fp8_f32 v7, v12, v13 op_sel:[0,0,1]
	v_mul_f32_e32 v12, v49, v15
	v_mul_f32_e32 v13, v53, v15
	v_cvt_pk_fp8_f32 v10, v0, v11
	v_mov_b32_e32 v11, v1
	v_cvt_pk_fp8_f32 v11, v12, v13
	v_mul_f32_e32 v80, v83, v15
	v_mul_f32_e32 v81, v87, v15
	v_mov_b32_e32 v5, v1
	v_cvt_pk_fp8_f32 v5, v80, v81
	v_mul_f32_e32 v14, v66, v15
	v_mul_f32_e32 v64, v70, v15
	v_mul_f32_e32 v67, v67, v15
	v_mul_f32_e32 v68, v71, v15
	v_mov_b32_e32 v8, v1
	v_mov_b32_e32 v9, v1
	v_cvt_pk_fp8_f32 v8, v14, v64
	v_cvt_pk_fp8_f32 v9, v67, v68
	v_mul_f32_e32 v14, v56, v15
	v_mul_f32_e32 v48, v60, v15
	v_mul_f32_e32 v49, v57, v15
	v_mul_f32_e32 v52, v61, v15
	v_mul_f32_e32 v50, v50, v15
	v_mul_f32_e32 v53, v54, v15
	v_mul_f32_e32 v51, v51, v15
	v_mul_f32_e32 v55, v55, v15
	v_mov_b32_e32 v12, v1
	v_mov_b32_e32 v13, v1
	v_cvt_pk_fp8_f32 v12, v50, v53
	v_cvt_pk_fp8_f32 v13, v51, v55
	v_cvt_pk_fp8_f32 v10, v14, v48 op_sel:[0,0,1]
	v_cvt_pk_fp8_f32 v11, v49, v52 op_sel:[0,0,1]
	v_mul_f32_e32 v0, v32, v15
	v_mul_f32_e32 v14, v36, v15
	v_mul_f32_e32 v36, v40, v15
	v_mul_f32_e32 v40, v44, v15
	v_mul_f32_e32 v44, v33, v15
	v_mul_f32_e32 v37, v37, v15
	v_mul_f32_e32 v48, v34, v15
	v_mul_f32_e32 v38, v38, v15
	v_mul_f32_e32 v49, v35, v15
	v_mul_f32_e32 v39, v39, v15
	v_mov_b32_e32 v32, v1
	v_mov_b32_e32 v33, v1
	v_mov_b32_e32 v34, v1
	v_mov_b32_e32 v35, v1
	v_mul_f32_e32 v82, v91, v15
	v_mul_f32_e32 v83, v95, v15
	v_cvt_pk_fp8_f32 v32, v0, v14
	v_cvt_pk_fp8_f32 v33, v44, v37
	v_cvt_pk_fp8_f32 v34, v48, v38
	v_cvt_pk_fp8_f32 v35, v49, v39
	v_cvt_pk_fp8_f32 v5, v82, v83 op_sel:[0,0,1]
	v_mul_f32_e32 v65, v74, v15
	v_mul_f32_e32 v66, v78, v15
	v_mul_f32_e32 v69, v75, v15
	v_mul_f32_e32 v70, v79, v15
	v_cvt_pk_fp8_f32 v8, v65, v66 op_sel:[0,0,1]
	v_cvt_pk_fp8_f32 v9, v69, v70 op_sel:[0,0,1]
	v_mul_f32_e32 v54, v58, v15
	v_mul_f32_e32 v56, v62, v15
	v_mul_f32_e32 v57, v59, v15
	v_mul_f32_e32 v58, v63, v15
	v_cvt_pk_fp8_f32 v12, v54, v56 op_sel:[0,0,1]
	v_cvt_pk_fp8_f32 v13, v57, v58 op_sel:[0,0,1]
	v_mul_f32_e32 v41, v41, v15
	v_mul_f32_e32 v45, v45, v15
	v_mul_f32_e32 v42, v42, v15
	v_mul_f32_e32 v46, v46, v15
	v_mul_f32_e32 v43, v43, v15
	v_mul_f32_e32 v15, v47, v15
	v_cvt_pk_fp8_f32 v32, v36, v40 op_sel:[0,0,1]
	v_cvt_pk_fp8_f32 v33, v41, v45 op_sel:[0,0,1]
	v_cvt_pk_fp8_f32 v34, v42, v46 op_sel:[0,0,1]
	v_cvt_pk_fp8_f32 v35, v43, v15 op_sel:[0,0,1]
	global_store_dwordx4 v[96:97], v[2:5], off
	global_store_dwordx4 v[96:97], v[6:9], off offset:32
	global_store_dwordx4 v[96:97], v[10:13], off offset:64
	global_store_dwordx4 v[96:97], v[32:35], off offset:96
	s_mov_b32 s91, 8

.LBB0_1442:
	s_andn2_b64 vcc, exec, s[62:63]
	s_cbranch_vccnz .LBB0_1431
	v_lshl_add_u32 v0, v248, 2, s29
	ds_read2st64_b32 v[6:7], v0 offset0:224 offset1:240
	v_mov_b32_e32 v2, v1
	s_lshl_b32 s56, s56, 7
	s_waitcnt lgkmcnt(0)
	v_mul_f32_e32 v3, v16, v7
	v_mul_f32_e32 v4, v20, v7
	v_cvt_pk_fp8_f32 v2, v3, v4
	v_mul_f32_e32 v4, v17, v7
	v_mul_f32_e32 v8, v21, v7
	v_mov_b32_e32 v3, v1
	v_cvt_pk_fp8_f32 v3, v4, v8
	v_mov_b32_e32 v0, v6
	v_mul_f32_e32 v5, v24, v7
	v_mul_f32_e32 v6, v28, v7
	v_cvt_pk_fp8_f32 v2, v5, v6 op_sel:[0,0,1]
	v_mul_f32_e32 v4, v25, v7
	v_mul_f32_e32 v5, v29, v7
	v_cvt_pk_fp8_f32 v3, v4, v5 op_sel:[0,0,1]
	v_mul_f32_e32 v5, v18, v7
	v_mul_f32_e32 v6, v22, v7
	v_mov_b32_e32 v4, v1
	v_cvt_pk_fp8_f32 v4, v5, v6
	v_mul_f32_e32 v6, v19, v7
	v_mul_f32_e32 v10, v23, v7
	v_mov_b32_e32 v5, v1
	v_cvt_pk_fp8_f32 v5, v6, v10
	v_mul_f32_e32 v8, v26, v7
	v_mul_f32_e32 v9, v30, v7
	v_mul_f32_e32 v6, v27, v7
	v_mul_f32_e32 v7, v31, v7
	v_cvt_pk_fp8_f32 v5, v6, v7 op_sel:[0,0,1]
	v_lshlrev_b64 v[6:7], 10, v[0:1]
	v_cvt_pk_fp8_f32 v4, v8, v9 op_sel:[0,0,1]
	v_lshl_add_u64 v[6:7], s[12:13], 0, v[6:7]
	v_lshl_add_u64 v[6:7], v[6:7], 0, s[56:57]
	v_lshl_add_u64 v[6:7], v[6:7], 0, s[34:35]
	v_lshl_add_u64 v[6:7], v[6:7], 0, v[218:219]
	global_store_dwordx4 v[6:7], v[2:5], off
	s_mov_b32 s92, 1
	s_branch .LBB0_1431
